# speedup vs baseline: 1.0185x; 1.0092x over previous
.LBB1_37:
	v_or_b32_e32 v12, s6, v1
	v_max_f32_e32 v15, v10, v10
	v_mul_u32_u24_e32 v10, 44, v12
	v_max_f32_e32 v13, v11, v11
	v_max_f32_e32 v14, v9, v9
	v_max_f32_e32 v16, v7, v7
	v_max_f32_e32 v17, v8, v8
	v_max_f32_e32 v18, v6, v6
	v_max_f32_e32 v19, v4, v4
	v_max_f32_e32 v20, v5, v5
	v_max_f32_e32 v21, v2, v2
	v_max_f32_e32 v22, v3, v3
	ds_read2_b32 v[2:3], v10 offset0:6 offset1:7
	ds_read2_b32 v[4:5], v10 offset0:2 offset1:3
	ds_read2_b32 v[6:7], v10 offset0:4 offset1:5
	ds_read2_b32 v[8:9], v10 offset0:8 offset1:9
	ds_read2_b32 v[10:11], v10 offset1:1
	s_waitcnt lgkmcnt(4)
	v_max_f32_e32 v3, v3, v3
	v_max_f32_e32 v2, v2, v2
	s_waitcnt lgkmcnt(3)
	v_max_f32_e32 v5, v5, v5
	s_waitcnt lgkmcnt(1)
	v_max_f32_e32 v9, v9, v9
	v_max_f32_e32 v8, v8, v8
	v_max_f32_e32 v7, v7, v7
	s_waitcnt lgkmcnt(0)
	v_max_f32_e32 v11, v11, v11
	v_max_f32_e32 v4, v4, v4
	v_max_f32_e32 v6, v6, v6
	v_max_f32_e32 v10, v10, v10
	v_min_f32_e32 v3, v13, v3
	v_min_f32_e32 v9, v17, v9
	v_min_f32_e32 v2, v18, v2
	v_min_f32_e32 v8, v22, v8
	v_max_f32_e32 v12, v15, v5
	v_max_f32_e32 v13, v16, v7
	v_max_f32_e32 v17, v20, v4
	v_max_f32_e32 v18, v21, v6
	v_min_f32_e32 v5, v15, v5
	v_min_f32_e32 v7, v16, v7
	v_min_f32_e32 v4, v20, v4
	v_min_f32_e32 v6, v21, v6
	v_max_f32_e32 v15, v14, v3
	v_max_f32_e32 v16, v9, v11
	v_max_f32_e32 v20, v19, v2
	v_max_f32_e32 v21, v8, v10
	v_min_f32_e32 v3, v14, v3
	v_min_f32_e32 v9, v9, v11
	v_min_f32_e32 v2, v19, v2
	v_min_f32_e32 v8, v8, v10
	v_min_f32_e32 v10, v3, v5
	v_min_f32_e32 v11, v7, v9
	v_min_f32_e32 v14, v2, v4
	v_min_f32_e32 v19, v6, v8
	v_max_f32_e32 v3, v3, v5
	v_max_f32_e32 v5, v7, v9
	v_max_f32_e32 v2, v2, v4
	v_max_f32_e32 v4, v6, v8
	v_min_f32_e32 v6, v13, v16
	v_min_f32_e32 v7, v18, v21
	v_min_f32_e32 v8, v10, v11
	v_min_f32_e32 v13, v14, v19
	v_max_f32_e32 v10, v10, v11
	v_max_f32_e32 v11, v14, v19
	v_min_f32_e32 v14, v3, v5
	v_min_f32_e32 v16, v2, v4
	v_max_f32_e32 v3, v3, v5
	v_max_f32_e32 v18, v2, v4
	v_min3_f32 v6, v15, v12, v6
	v_min3_f32 v12, v20, v17, v7
	s_movk_i32 s6, 0x80
	s_and_b64 vcc, exec, s[4:5]
	s_mov_b64 s[4:5], 0
	v_min_f32_e32 v9, v8, v13
	v_max_f32_e32 v4, v8, v13
	v_min_f32_e32 v7, v10, v11
	v_max_f32_e32 v2, v10, v11
	v_min_f32_e32 v10, v14, v16
	v_max_f32_e32 v5, v14, v16
	v_min_f32_e32 v8, v3, v18
	v_max_f32_e32 v3, v3, v18
	v_min_f32_e32 v11, v6, v12
	v_max_f32_e32 v6, v6, v12
	s_cbranch_vccnz .LBB1_37
	v_or_b32_e32 v12, s33, v1
	s_movk_i32 s4, 0x400
	v_mov_b32_e32 v13, 0x1e0000
	v_cmp_gt_i32_e32 vcc, s4, v12
	s_lshl_b32 s4, s8, 2
	v_mov_b32_e32 v15, 0
	v_cndmask_b32_e64 v14, v13, 0, vcc
	s_add_i32 s4, s4, s76
	s_mov_b32 s5, 0
	v_lshl_add_u64 v[16:17], s[70:71], 0, v[14:15]
	s_mul_i32 s4, s4, 12
	v_cndmask_b32_e64 v14, 13, 10, vcc
	v_lshlrev_b64 v[18:19], v14, s[4:5]
	v_lshl_add_u64 v[16:17], v[18:19], 2, v[16:17]
	v_ashrrev_i32_e32 v13, 31, v12
	v_lshl_add_u64 v[12:13], v[12:13], 2, v[16:17]
	v_lshlrev_b64 v[16:17], v14, 1
	v_lshl_add_u64 v[16:17], v[16:17], 2, v[12:13]
	global_store_dword v[16:17], v4, off sc1
	v_lshlrev_b64 v[16:17], v14, 2
	v_lshl_add_u64 v[16:17], v[16:17], 2, v[12:13]
	global_store_dword v[16:17], v7, off sc1
	v_lshlrev_b64 v[16:17], v14, 3
	v_lshl_add_u64 v[16:17], v[16:17], 2, v[12:13]
	global_store_dword v[16:17], v2, off sc1
	v_lshlrev_b64 v[16:17], v14, 4
	v_lshl_add_u64 v[16:17], v[16:17], 2, v[12:13]
	global_store_dword v[16:17], v10, off sc1
	v_lshlrev_b64 v[16:17], v14, 5
	v_lshl_add_u64 v[16:17], v[16:17], 2, v[12:13]
	global_store_dword v[16:17], v5, off sc1
	v_lshlrev_b64 v[4:5], v14, 6
	v_lshl_add_u64 v[4:5], v[4:5], 2, v[12:13]
	global_store_dword v[4:5], v8, off sc1
	v_lshlrev_b64 v[4:5], v14, 7
	v_lshl_add_u64 v[4:5], v[4:5], 2, v[12:13]
	global_store_dword v[4:5], v3, off sc1
	v_lshlrev_b64 v[2:3], v14, 8
	v_lshl_add_u64 v[2:3], v[2:3], 2, v[12:13]
	global_store_dword v[2:3], v11, off sc1
	v_lshlrev_b64 v[2:3], v14, 9
	v_lshl_add_u64 v[2:3], v[2:3], 2, v[12:13]
	global_store_dword v[2:3], v6, off sc1
	v_mov_b32_e32 v2, 0x58000
	v_mov_b32_e32 v3, 0xb000
	v_cndmask_b32_e32 v14, v2, v3, vcc
	v_lshl_add_u64 v[2:3], v[12:13], 0, v[14:15]
	global_store_dword v[12:13], v9, off sc1
	global_store_dword v[2:3], v116, off sc1
